# scan sequence split over FOUR CUs (one MFMA wave per CU, 64 scan WGs), helpers WGs 64..95
# baseline (speedup 1.0000x reference)
; DI void gdn_scan_seq(const Params& p, int bh16, char* ldsf) {
;     ...
;   f32x16 S[4];
; #pragma unroll
;   for (int m = 0; m < 4; ++m)
; #pragma unroll
;     for (int r = 0; r < 16; ++r) S[m][r] = 0.f;
;   asm volatile("s_waitcnt vmcnt(0)" ::: "memory");
;   __syncthreads();
;   SCAN_ISSUE(0, 0); SCAN_ISSUE(1, 1);
; DI void phase_mixer(const Params& p, int bid, int nb, char* lds, char* ctl, char* ldsf) {
;     ...
;   if (bid < 32) { if (vb == 0) gdn_scan_seq(p, bid >> 1, ldsf); else { __syncthreads(); for (int k = 0; k < 128; ++k) { __builtin_amdgcn_s_barrier(); asm volatile("" ::: "memory"); } __syncthreads(); } }
.LBB0_1207:
	s_or_b64 exec, exec, s[0:1]
	v_mov_b32_e32 v135, v206
	s_waitcnt lgkmcnt(0)
	s_barrier
	s_movk_i32 s2, 128
	v_cmp_gt_i32_e64 s[6:7], s2, v176
	s_nop 3
	s_and_saveexec_b64 s[0:1], s[6:7]
	s_cbranch_execz .LBB0_1227
	s_movk_i32 s2, 0xff
	v_cmp_lt_u32_e32 vcc, s2, v207
	s_and_saveexec_b64 s[2:3], vcc
	s_xor_b64 s[6:7], exec, s[2:3]
	s_cbranch_execz .LBB0_1212
	v_readlane_b32 s2, v250, 0
	v_lshrrev_b32_e32 v209, 6, v206
	v_and_b32_e32 v208, 63, v206
	v_lshlrev_b32_e32 v132, 12, v209
	v_lshl_or_b32 v132, v208, 4, v132
	v_readfirstlane_b32 s3, v209
	s_nop 3
	s_lshr_b32 s18, s2, 4
	s_and_b32 s2, s2, 15
	s_cmp_lt_u32 s3, 1
	s_cselect_b64 s[16:17], -1, 0
	v_and_b32_e32 v209, 0, v209
	v_lshl_add_u32 v209, s18, 0, v209
	v_lshlrev_b32_e32 v133, 11, v209
	v_lshl_or_b32 v133, v208, 5, v133
	v_add_u32_e32 v134, 0x2000, v133
	v_lshlrev_b32_e32 v210, 12, v209
	v_lshl_or_b32 v210, v208, 4, v210
	v_mov_b32_e32 v208, v132
	s_lshl_b32 s2, s2, 21
	s_add_u32 s8, s84, s2
	s_addc_u32 s9, s85, 0
	s_add_u32 s12, s8, 0x1c000000
	s_addc_u32 s13, s9, 0
	s_add_u32 s8, s8, 0x1e000000
	s_addc_u32 s9, s9, 0
	s_add_u32 s10, s66, s2
	s_addc_u32 s11, s67, 0
	s_add_u32 s10, s10, 0x2000000
	s_addc_u32 s11, s11, 0
	s_mov_b32 s15, 0
	global_load_dwordx4 v[0:3], v132, s[8:9]
	global_load_dwordx4 v[4:7], v132, s[8:9] offset:1024
	global_load_dwordx4 v[8:11], v132, s[8:9] offset:2048
	global_load_dwordx4 v[12:15], v132, s[8:9] offset:3072
	global_load_dwordx4 v[16:19], v132, s[10:11]
	global_load_dwordx4 v[20:23], v132, s[10:11] offset:1024
	global_load_dwordx4 v[24:27], v132, s[10:11] offset:2048
	global_load_dwordx4 v[28:31], v132, s[10:11] offset:3072
	global_load_dwordx4 v[32:35], v133, s[12:13]
	global_load_dwordx4 v[36:39], v133, s[12:13] offset:16
	global_load_dwordx4 v[40:43], v134, s[12:13]
	global_load_dwordx4 v[44:47], v134, s[12:13] offset:16
	s_add_u32 s15, s15, 1
	s_cmp_lt_u32 s15, 0x80
	s_cselect_b32 s14, 0x4000, 0
	s_add_u32 s8, s8, s14
	s_addc_u32 s9, s9, 0
	s_add_u32 s10, s10, s14
	s_addc_u32 s11, s11, 0
	s_add_u32 s12, s12, s14
	s_addc_u32 s13, s13, 0
	global_load_dwordx4 v[48:51], v132, s[8:9]
	global_load_dwordx4 v[52:55], v132, s[8:9] offset:1024
	global_load_dwordx4 v[56:59], v132, s[8:9] offset:2048
	global_load_dwordx4 v[60:63], v132, s[8:9] offset:3072
	global_load_dwordx4 v[64:67], v132, s[10:11]
	global_load_dwordx4 v[68:71], v132, s[10:11] offset:1024
	global_load_dwordx4 v[72:75], v132, s[10:11] offset:2048
	global_load_dwordx4 v[76:79], v132, s[10:11] offset:3072
	global_load_dwordx4 v[80:83], v133, s[12:13]
	global_load_dwordx4 v[84:87], v133, s[12:13] offset:16
	global_load_dwordx4 v[88:91], v134, s[12:13]
	global_load_dwordx4 v[92:95], v134, s[12:13] offset:16
	s_add_u32 s15, s15, 1
	s_cmp_lt_u32 s15, 0x80
	s_cselect_b32 s14, 0x4000, 0
	s_add_u32 s8, s8, s14
	s_addc_u32 s9, s9, 0
	s_add_u32 s10, s10, s14
	s_addc_u32 s11, s11, 0
	s_add_u32 s12, s12, s14
	s_addc_u32 s13, s13, 0
	global_load_dwordx4 v[96:99], v132, s[8:9]
	global_load_dwordx4 v[100:103], v132, s[8:9] offset:1024
	global_load_dwordx4 v[104:107], v132, s[8:9] offset:2048
	global_load_dwordx4 v[108:111], v132, s[8:9] offset:3072
	global_load_dwordx4 v[112:115], v132, s[10:11]
	global_load_dwordx4 v[116:119], v132, s[10:11] offset:1024
	global_load_dwordx4 v[120:123], v132, s[10:11] offset:2048
	global_load_dwordx4 v[124:127], v132, s[10:11] offset:3072
	global_load_dwordx4 v[128:131], v133, s[12:13]
	global_load_dwordx4 v[136:139], v133, s[12:13] offset:16
	global_load_dwordx4 v[140:143], v134, s[12:13]
	global_load_dwordx4 v[148:151], v134, s[12:13] offset:16
	s_add_u32 s15, s15, 1
	s_cmp_lt_u32 s15, 0x80
	s_cselect_b32 s14, 0x4000, 0
	s_add_u32 s8, s8, s14
	s_addc_u32 s9, s9, 0
	s_add_u32 s10, s10, s14
	s_addc_u32 s11, s11, 0
	s_add_u32 s12, s12, s14
	s_addc_u32 s13, s13, 0
	global_load_dwordx4 v[152:155], v132, s[8:9]
	global_load_dwordx4 v[156:159], v132, s[8:9] offset:1024
	global_load_dwordx4 v[160:163], v132, s[8:9] offset:2048
	global_load_dwordx4 v[164:167], v132, s[8:9] offset:3072
	global_load_dwordx4 v[168:171], v132, s[10:11]
	global_load_dwordx4 v[172:175], v132, s[10:11] offset:1024
	global_load_dwordx4 v[178:181], v132, s[10:11] offset:2048
	global_load_dwordx4 v[182:185], v132, s[10:11] offset:3072
	global_load_dwordx4 v[190:193], v133, s[12:13]
	global_load_dwordx4 v[194:197], v133, s[12:13] offset:16
	global_load_dwordx4 v[198:201], v134, s[12:13]
	global_load_dwordx4 v[202:205], v134, s[12:13] offset:16
	s_add_u32 s15, s15, 1
	s_cmp_lt_u32 s15, 0x80
	s_cselect_b32 s14, 0x4000, 0
	s_add_u32 s8, s8, s14
	s_addc_u32 s9, s9, 0
	s_add_u32 s10, s10, s14
	s_addc_u32 s11, s11, 0
	s_add_u32 s12, s12, s14
	s_addc_u32 s13, s13, 0
	s_mov_b32 s2, 0
	s_mov_b32 s3, 0
	s_barrier

; DI int tidx() { int t = threadIdx.x & 255; asm volatile("" : "+v"(t)); return t; }
; DI void gdn_scan_seq(const Params& p, int bh16, char* ldsf) {
;   const int tid = tidx(), lane = tid & 63, wv = tid >> 6;
;   const float* glp = (const float*)(p.ws + WS_GL) + bh16 * 128;
;   const char* wf = (const char*)(p.ws + WS_WF) + (size_t)bh16 * 128 * 16384 + tid * 16;
;   const char* kf = (const char*)p.out + 32 * MiB + (size_t)bh16 * 128 * 16384 + tid * 16;
;   const char* uf = (const char*)(p.ws + WS_UF) + (size_t)bh16 * 128 * 16384 + (size_t)(wv * 64 + lane) * 32;
;   char* scp = p.ws + WS_SC + (size_t)bh16 * 128 * 32768 + (size_t)wv * 8192 + lane * 16;
;   float* glt = (float*)(ldsf + 2 * LDS_BYTES + 64);
;   if (tid < 128) glt[tid] = glp[tid];
;     ...
;   f32x16 S[4];
; #pragma unroll
;   for (int m = 0; m < 4; ++m)
; #pragma unroll
;     for (int r = 0; r < 16; ++r) S[m][r] = 0.f;
;   asm volatile("s_waitcnt vmcnt(0)" ::: "memory");
;   __syncthreads();
;   SCAN_ISSUE(0, 0); SCAN_ISSUE(1, 1);
;   int sl = 0;
.LBB0_1212:
	s_andn2_saveexec_b64 s[2:3], s[6:7]
	s_cbranch_execz .LBB0_1226
	v_readlane_b32 s2, v250, 0
	v_lshrrev_b32_e32 v0, 6, v206
	v_and_b32_e32 v1, 63, v206
	v_lshlrev_b32_e32 v130, 4, v1
	v_readfirstlane_b32 s16, v206
	s_nop 3
	s_lshr_b32 s17, s2, 4
	s_and_b32 s2, s2, 15
	v_lshl_add_u32 v0, s17, 0, v0
	v_lshl_add_u32 v129, v0, 12, v130
	v_lshl_add_u32 v128, v0, 13, v130
	s_lshl_b32 s3, s2, 9
	s_add_u32 s12, s84, s3
	s_addc_u32 s13, s85, 0
	s_add_u32 s12, s12, 0x1a00000
	s_addc_u32 s13, s13, 0
	v_cmp_gt_u32_e32 vcc, 0x80, v206
	s_and_saveexec_b64 s[6:7], vcc
	s_cbranch_execz .Lscan_glt_done
	v_lshlrev_b32_e32 v2, 2, v206
	global_load_dword v3, v2, s[12:13]
	v_add_u32_e32 v2, 0x24040, v2
	s_waitcnt vmcnt(0)
	ds_write_b32 v2, v3
.Lscan_glt_done:
	s_or_b64 exec, exec, s[6:7]
	s_cmp_ge_u32 s16, 0x40
	s_cbranch_scc1 .Lscan_idle
	s_lshl_b32 s3, s2, 22
	s_add_u32 s8, s56, s3
	s_addc_u32 s9, s57, 0
	s_add_u32 s10, s8, 0x1000
	s_addc_u32 s11, s9, 0
	v_mov_b32_e32 v0, 0
	v_mov_b32_e32 v1, 0
	v_mov_b32_e32 v2, 0
	v_mov_b32_e32 v3, 0
	v_mov_b32_e32 v4, 0
	v_mov_b32_e32 v5, 0
	v_mov_b32_e32 v6, 0
	v_mov_b32_e32 v7, 0
	v_mov_b32_e32 v8, 0
	v_mov_b32_e32 v9, 0
	v_mov_b32_e32 v10, 0
	v_mov_b32_e32 v11, 0
	v_mov_b32_e32 v12, 0
	v_mov_b32_e32 v13, 0
	v_mov_b32_e32 v14, 0
	v_mov_b32_e32 v15, 0
	v_mov_b32_e32 v16, 0
	v_mov_b32_e32 v17, 0
	v_mov_b32_e32 v18, 0
	v_mov_b32_e32 v19, 0
	v_mov_b32_e32 v20, 0
	v_mov_b32_e32 v21, 0
	v_mov_b32_e32 v22, 0
	v_mov_b32_e32 v23, 0
	v_mov_b32_e32 v24, 0
	v_mov_b32_e32 v25, 0
	v_mov_b32_e32 v26, 0
	v_mov_b32_e32 v27, 0
	v_mov_b32_e32 v28, 0
	v_mov_b32_e32 v29, 0
	v_mov_b32_e32 v30, 0
	v_mov_b32_e32 v31, 0
	v_mov_b32_e32 v32, 0
	v_mov_b32_e32 v33, 0
	v_mov_b32_e32 v34, 0
	v_mov_b32_e32 v35, 0
	v_mov_b32_e32 v36, 0
	v_mov_b32_e32 v37, 0
	v_mov_b32_e32 v38, 0
	v_mov_b32_e32 v39, 0
	v_mov_b32_e32 v40, 0
	v_mov_b32_e32 v41, 0
	v_mov_b32_e32 v42, 0
	v_mov_b32_e32 v43, 0
	v_mov_b32_e32 v44, 0
	v_mov_b32_e32 v45, 0
	v_mov_b32_e32 v46, 0
	v_mov_b32_e32 v47, 0
	v_mov_b32_e32 v48, 0
	v_mov_b32_e32 v49, 0
	v_mov_b32_e32 v50, 0
	v_mov_b32_e32 v51, 0
	v_mov_b32_e32 v52, 0
	v_mov_b32_e32 v53, 0
	v_mov_b32_e32 v54, 0
	v_mov_b32_e32 v55, 0
	v_mov_b32_e32 v56, 0
	v_mov_b32_e32 v57, 0
	v_mov_b32_e32 v58, 0
	v_mov_b32_e32 v59, 0
	v_mov_b32_e32 v60, 0
	v_mov_b32_e32 v61, 0
	v_mov_b32_e32 v62, 0
	v_mov_b32_e32 v63, 0
	v_mov_b32_e32 v80, 0
	v_mov_b32_e32 v81, 0
	v_mov_b32_e32 v82, 0
	v_mov_b32_e32 v83, 0
	v_mov_b32_e32 v84, 0
	v_mov_b32_e32 v85, 0
	v_mov_b32_e32 v86, 0
	v_mov_b32_e32 v87, 0
	v_mov_b32_e32 v182, 0
	v_mov_b32_e32 v183, 0
	v_mov_b32_e32 v184, 0
	v_mov_b32_e32 v185, 0
	v_mov_b32_e32 v190, 0
	v_mov_b32_e32 v191, 0
	v_mov_b32_e32 v192, 0
	v_mov_b32_e32 v193, 0
	v_mov_b32_e32 v194, 0
	v_mov_b32_e32 v195, 0
	v_mov_b32_e32 v196, 0
	v_mov_b32_e32 v197, 0
	v_mov_b32_e32 v198, 0
	v_mov_b32_e32 v199, 0
	v_mov_b32_e32 v200, 0
	v_mov_b32_e32 v201, 0
	v_mov_b32_e32 v202, 0
	v_mov_b32_e32 v203, 0
	v_mov_b32_e32 v204, 0
	v_mov_b32_e32 v205, 0
	v_mov_b32_e32 v208, 0
	v_mov_b32_e32 v209, 0
	v_mov_b32_e32 v210, 0
	v_mov_b32_e32 v211, 0
	v_mov_b32_e32 v212, 0
	v_mov_b32_e32 v213, 0
	v_mov_b32_e32 v214, 0
	v_mov_b32_e32 v215, 0
	v_mov_b32_e32 v216, 0
	v_mov_b32_e32 v217, 0
	v_mov_b32_e32 v218, 0
	v_mov_b32_e32 v219, 0
	s_or_b32 s16, s16, s17
	s_lshl_b32 s3, s2, 6
	s_add_u32 s14, s84, s3
	s_addc_u32 s15, s85, 0
	s_add_u32 s14, s14, 0xc00
	s_addc_u32 s15, s15, 0
	v_mov_b32_e32 v132, 1
	v_mov_b32_e32 v133, 0
	s_mov_b32 s2, 0
	s_mov_b32 s3, 0
	s_mov_b32 s18, 0x24040
	s_waitcnt lgkmcnt(0)
	s_barrier

; #define LAS __attribute__((address_space(3)))
; DI int tidx() { int t = threadIdx.x & 255; asm volatile("" : "+v"(t)); return t; }
; DI void phase_mixer(const Params& p, int bid, int nb, char* lds, char* ctl, char* ldsf) {
;   const int vb = threadIdx.x >> 8, lane = tidx() & 63;
;   if (bid < 32) { if (vb == 0) gdn_scan_seq(p, bid >> 1, ldsf); else { __syncthreads(); for (int k = 0; k < 128; ++k) { __builtin_amdgcn_s_barrier(); asm volatile("" ::: "memory"); } __syncthreads(); } }
;   unsigned* ctr = (unsigned*)(p.ws + WS_CTL);
;   volatile LAS int* slot = (volatile LAS int*)(ctl + 16 + 4 * vb);
;   volatile LAS unsigned* hbc = (volatile LAS unsigned*)(ctl + 32 + 4 * vb);
;   unsigned hbph = 0u;
.LBB0_1226:
.LBB0_1227:
	s_or_b64 exec, exec, s[0:1]
	v_readlane_b32 s2, v250, 0
	v_readfirstlane_b32 s3, v207
	s_nop 3
	s_sub_u32 s14, s2, 64
	s_cmp_lt_u32 s14, 32
	s_cbranch_scc0 .Lpf_done
	s_and_b32 s15, s3, 0xff
	s_cmp_eq_u32 s15, 0
	s_cbranch_scc0 .Lpf_done
	s_lshr_b32 s24, s14, 3
	s_and_b32 s14, s14, 7
	s_lshr_b32 s15, s3, 8
	s_lshl_b32 s15, s15, 3
	s_add_u32 s14, s14, s15
	s_lshl_b32 s15, s14, 21
	s_lshl_b32 s3, s24, 14
	s_add_u32 s15, s15, s3
	s_add_u32 s16, s84, s15
	s_addc_u32 s17, s85, 0
	s_add_u32 s18, s16, 0x1c000000
	s_addc_u32 s19, s17, 0
	s_add_u32 s16, s16, 0x1e000000
	s_addc_u32 s17, s17, 0
	s_add_u32 s22, s66, s15
	s_addc_u32 s23, s67, 0
	s_add_u32 s22, s22, 0x2000000
	s_addc_u32 s23, s23, 0
	s_lshl_b32 s15, s14, 6
	s_add_u32 s2, s84, s15
	s_addc_u32 s3, s85, 0
	s_add_u32 s2, s2, 0xc00
	s_addc_u32 s3, s3, 0
	v_mbcnt_lo_u32_b32 v0, -1, 0
	v_mbcnt_hi_u32_b32 v0, -1, v0
	v_lshlrev_b32_e32 v0, 7, v0
	v_add_u32_e32 v111, 0x2000, v0
	v_mov_b32_e32 v1, 0
	s_mov_b32 s14, s24
	s_mov_b32 s24, 0
